# instruction selection: mix_unit depthwise conv accumulates two taps per v_pk_fma_f32 (odd outputs use a one-register-shifted copy of the weights); 496 scalar FMAs become 232 packed + 32 scalar + 28 mo
# speedup vs baseline: 1.0069x; 1.0028x over previous
.LBB0_407:
	ds_read_b128 v[18:21], v13
	ds_read_b128 v[22:25], v13 offset:16
	v_add_u32_e32 v12, -1, v12
	v_cmp_eq_u32_e32 vcc, 0, v12
	v_add_u32_e32 v13, 0xfffffc00, v13
	s_or_b64 s[0:1], vcc, s[0:1]
	s_waitcnt lgkmcnt(1)
	v_pk_add_f32 v[6:7], v[6:7], v[18:19]
	v_pk_add_f32 v[8:9], v[8:9], v[20:21]
	s_waitcnt lgkmcnt(0)
	v_pk_add_f32 v[10:11], v[10:11], v[22:23]
	v_pk_add_f32 v[2:3], v[2:3], v[24:25]
	s_andn2_b64 exec, exec, s[0:1]
	s_cbranch_execnz .LBB0_407
	s_or_b64 exec, exec, s[0:1]
	ds_read_b128 v[18:21], v14 offset:40992
	ds_read_b128 v[22:25], v14 offset:41008
	v_readlane_b32 s36, v251, 20
	v_readlane_b32 s42, v251, 26
	v_readlane_b32 s43, v251, 27
	s_waitcnt lgkmcnt(1)
	v_pk_fma_f32 v[6:7], v[4:5], v[6:7], v[18:19] neg_lo:[0,0,1] neg_hi:[0,0,1]
	v_pk_fma_f32 v[8:9], v[4:5], v[8:9], v[20:21] neg_lo:[0,0,1] neg_hi:[0,0,1]
	s_waitcnt lgkmcnt(0)
	v_pk_fma_f32 v[10:11], v[4:5], v[10:11], v[22:23] neg_lo:[0,0,1] neg_hi:[0,0,1]
	v_pk_fma_f32 v[12:13], v[4:5], v[2:3], v[24:25] neg_lo:[0,0,1] neg_hi:[0,0,1]
	v_cvt_pk_bf16_f32 v2, v6, v7
	v_cvt_pk_bf16_f32 v3, v8, v9
	v_cvt_pk_bf16_f32 v4, v10, v11
	v_cvt_pk_bf16_f32 v5, v12, v13
	ds_write_b128 v15, v[2:5] offset:16
	v_or_b32_sdwa v4, v93, s54 dst_sel:DWORD dst_unused:UNUSED_PAD src0_sel:BYTE_0 src1_sel:DWORD
	v_mov_b32_e32 v5, v115
	v_mov_b32_e32 v2, 2
	v_lshl_add_u64 v[4:5], v[4:5], 2, s[42:43]
	v_lshlrev_b32_sdwa v114, v2, v93 dst_sel:DWORD dst_unused:UNUSED_PAD src0_sel:DWORD src1_sel:BYTE_0
	global_load_dword v42, v[4:5], off
	global_load_dword v50, v114, s[12:13]
	global_load_dword v51, v114, s[12:13] offset:1024
	global_load_dword v52, v114, s[12:13] offset:2048
	global_load_dword v53, v114, s[12:13] offset:3072
	v_lshl_add_u64 v[2:3], s[12:13], 0, v[114:115]
	s_movk_i32 s0, 0x1000
	v_add_co_u32_e32 v4, vcc, s0, v2
	s_movk_i32 s0, 0x2000
	s_nop 0
	v_addc_co_u32_e32 v5, vcc, 0, v3, vcc
	v_add_co_u32_e32 v6, vcc, s0, v2
	s_movk_i32 s0, 0x3000
	s_nop 0
	v_addc_co_u32_e32 v7, vcc, 0, v3, vcc
	global_load_dword v54, v[6:7], off offset:-4096
	global_load_dword v55, v[4:5], off offset:1024
	global_load_dword v56, v[4:5], off offset:2048
	global_load_dword v57, v[4:5], off offset:3072
	global_load_dword v58, v[6:7], off
	global_load_dword v59, v[6:7], off offset:1024
	global_load_dword v60, v[6:7], off offset:2048
	global_load_dword v61, v[6:7], off offset:3072
	v_add_co_u32_e32 v4, vcc, s0, v2
	s_movk_i32 s0, 0x4000
	s_nop 0
	v_addc_co_u32_e32 v5, vcc, 0, v3, vcc
	v_add_co_u32_e32 v6, vcc, s0, v2
	s_movk_i32 s0, 0x5000
	s_nop 0
	v_addc_co_u32_e32 v7, vcc, 0, v3, vcc
	global_load_dword v62, v[6:7], off offset:-4096
	global_load_dword v63, v[4:5], off offset:1024
	global_load_dword v64, v[4:5], off offset:2048
	global_load_dword v65, v[4:5], off offset:3072
	global_load_dword v66, v[6:7], off
	global_load_dword v67, v[6:7], off offset:1024
	global_load_dword v68, v[6:7], off offset:2048
	global_load_dword v69, v[6:7], off offset:3072
	v_add_co_u32_e32 v4, vcc, s0, v2
	s_movk_i32 s0, 0x6000
	s_nop 0
	v_addc_co_u32_e32 v5, vcc, 0, v3, vcc
	v_add_co_u32_e32 v6, vcc, s0, v2
	s_movk_i32 s0, 0x7000
	s_nop 0
	v_addc_co_u32_e32 v7, vcc, 0, v3, vcc
	global_load_dword v70, v[6:7], off offset:-4096
	global_load_dword v71, v[4:5], off offset:1024
	global_load_dword v72, v[4:5], off offset:2048
	global_load_dword v73, v[4:5], off offset:3072
	global_load_dword v74, v[6:7], off
	global_load_dword v75, v[6:7], off offset:1024
	global_load_dword v76, v[6:7], off offset:2048
	global_load_dword v77, v[6:7], off offset:3072
	v_add_co_u32_e32 v2, vcc, s0, v2
	v_and_b32_e32 v17, 0xfffff000, v16
	s_nop 0
	v_addc_co_u32_e32 v3, vcc, 0, v3, vcc
	global_load_dword v81, v[2:3], off
	global_load_dword v84, v[2:3], off offset:1024
	global_load_dword v85, v[2:3], off offset:2048
	v_or_b32_sdwa v2, v17, v93 dst_sel:DWORD dst_unused:UNUSED_PAD src0_sel:DWORD src1_sel:BYTE_0
	v_lshlrev_b32_e32 v43, 2, v2
	v_readlane_b32 s0, v254, 26
	v_or_b32_sdwa v16, v93, v16 dst_sel:DWORD dst_unused:UNUSED_PAD src0_sel:BYTE_0 src1_sel:DWORD
	s_ashr_i32 s18, s91, 1
	v_add_u32_e32 v18, s0, v43
	ds_read2st64_b32 v[14:15], v18 offset1:4
	ds_read2st64_b32 v[12:13], v18 offset0:8 offset1:12
	ds_read2st64_b32 v[10:11], v18 offset0:16 offset1:20
	ds_read2st64_b32 v[8:9], v18 offset0:24 offset1:28
	ds_read2st64_b32 v[6:7], v18 offset0:32 offset1:36
	ds_read2st64_b32 v[4:5], v18 offset0:40 offset1:44
	ds_read2st64_b32 v[2:3], v18 offset0:48 offset1:52
	ds_read_b32 v86, v18 offset:14336
	v_mov_b32_e32 v18, 0x3c00
	v_lshl_or_b32 v44, v16, 2, v18
	v_add_u32_e32 v16, s0, v44
	ds_read_b32 v87, v16
	v_lshlrev_b32_e32 v16, 2, v17
	v_add3_u32 v45, s0, v16, v114
	ds_read2st64_b32 v[30:31], v45 offset0:64 offset1:68
	ds_read2st64_b32 v[28:29], v45 offset0:72 offset1:76
	ds_read2st64_b32 v[26:27], v45 offset0:80 offset1:84
	ds_read2st64_b32 v[24:25], v45 offset0:88 offset1:92
	ds_read2st64_b32 v[22:23], v45 offset0:96 offset1:100
	ds_read2st64_b32 v[20:21], v45 offset0:104 offset1:108
	ds_read2st64_b32 v[16:17], v45 offset0:112 offset1:116
	ds_read2st64_b32 v[18:19], v45 offset0:120 offset1:124
	ds_read2st64_b32 v[32:33], v45 offset0:128 offset1:132
	ds_read2st64_b32 v[34:35], v45 offset0:136 offset1:140
	ds_read2st64_b32 v[36:37], v45 offset0:144 offset1:148
	ds_read2st64_b32 v[38:39], v45 offset0:152 offset1:156
	ds_read2st64_b32 v[40:41], v45 offset0:160 offset1:164
	ds_read2st64_b32 v[88:89], v45 offset0:168 offset1:172
	ds_read2st64_b32 v[48:49], v45 offset0:176 offset1:180
	s_lshl_b32 s2, s18, 12
	s_ashr_i32 s3, s2, 31
	s_lshl_b32 s0, s18, 6
	s_ashr_i32 s1, s0, 31
	s_lshl_b64 s[2:3], s[2:3], 1
	s_add_u32 s16, s24, s2
	s_addc_u32 s17, s25, s3
	v_lshlrev_b32_e32 v114, 7, v91
	s_waitcnt lgkmcnt(0)
	s_barrier
	s_lshl_b32 s2, s91, 4
	s_and_b32 s2, s2, 16
	s_lshl_b32 s3, s18, 7
	s_add_i32 s3, s3, 0
	s_add_i32 s3, s3, 0x12000
	v_readlane_b32 s37, v251, 21
	v_readlane_b32 s38, v251, 22
	v_readlane_b32 s39, v251, 23
	v_readlane_b32 s40, v251, 24
	v_readlane_b32 s41, v251, 25
	s_waitcnt vmcnt(0)
	v_mov_b32_e32 v212, v51
	v_mov_b32_e32 v213, v52
	v_mov_b32_e32 v214, v53
	v_mov_b32_e32 v215, v54
	v_mov_b32_e32 v216, v55
	v_mov_b32_e32 v217, v56
	v_mov_b32_e32 v218, v57
	v_mov_b32_e32 v219, v58
	v_mov_b32_e32 v220, v59
	v_mov_b32_e32 v221, v60
	v_mov_b32_e32 v222, v61
	v_mov_b32_e32 v223, v62
	v_mov_b32_e32 v234, v63
	v_mov_b32_e32 v235, v64
	v_mov_b32_e32 v236, v65
	v_mov_b32_e32 v237, v66
	v_mov_b32_e32 v238, v67
	v_mov_b32_e32 v239, v68
	v_mov_b32_e32 v240, v69
	v_mov_b32_e32 v241, v70
	v_mov_b32_e32 v242, v71
	v_mov_b32_e32 v243, v72
	v_mov_b32_e32 v244, v73
	v_mov_b32_e32 v245, v74
	v_mov_b32_e32 v246, v75
	v_mov_b32_e32 v247, v76
	v_mov_b32_e32 v248, v77
	v_mov_b32_e32 v249, v81
	v_fma_f32 v45, v50, v87, v42
	v_pk_mul_f32 v[230:231], v[212:213], v[30:31]
	v_pk_fma_f32 v[230:231], v[214:215], v[28:29], v[230:231]
	v_pk_fma_f32 v[230:231], v[216:217], v[26:27], v[230:231]
	v_pk_fma_f32 v[230:231], v[218:219], v[24:25], v[230:231]
	v_pk_fma_f32 v[230:231], v[220:221], v[22:23], v[230:231]
	v_pk_fma_f32 v[230:231], v[222:223], v[20:21], v[230:231]
	v_pk_fma_f32 v[230:231], v[234:235], v[16:17], v[230:231]
	v_pk_fma_f32 v[230:231], v[236:237], v[18:19], v[230:231]
	v_pk_fma_f32 v[230:231], v[238:239], v[32:33], v[230:231]
	v_pk_fma_f32 v[230:231], v[240:241], v[34:35], v[230:231]
	v_pk_fma_f32 v[230:231], v[242:243], v[36:37], v[230:231]
	v_pk_fma_f32 v[230:231], v[244:245], v[38:39], v[230:231]
	v_pk_fma_f32 v[230:231], v[246:247], v[40:41], v[230:231]
	v_pk_fma_f32 v[230:231], v[248:249], v[88:89], v[230:231]
	v_pk_fma_f32 v[230:231], v[84:85], v[48:49], v[230:231]
	v_add_f32_e32 v45, v45, v230
	v_add_f32_e32 v45, v45, v231
	v_fma_f32 v46, v85, v48, v42
	v_fmac_f32_e32 v46, v81, v88
	v_fmac_f32_e32 v46, v84, v89
	v_pk_mul_f32 v[230:231], v[50:51], v[86:87]
	v_pk_fma_f32 v[230:231], v[52:53], v[30:31], v[230:231]
	v_pk_fma_f32 v[230:231], v[54:55], v[28:29], v[230:231]
	v_pk_fma_f32 v[230:231], v[56:57], v[26:27], v[230:231]
	v_pk_fma_f32 v[230:231], v[58:59], v[24:25], v[230:231]
	v_pk_fma_f32 v[230:231], v[60:61], v[22:23], v[230:231]
	v_pk_fma_f32 v[230:231], v[62:63], v[20:21], v[230:231]
	v_pk_fma_f32 v[230:231], v[64:65], v[16:17], v[230:231]
	v_pk_fma_f32 v[230:231], v[66:67], v[18:19], v[230:231]
	v_pk_fma_f32 v[230:231], v[68:69], v[32:33], v[230:231]
	v_pk_fma_f32 v[230:231], v[70:71], v[34:35], v[230:231]
	v_pk_fma_f32 v[230:231], v[72:73], v[36:37], v[230:231]
	v_pk_fma_f32 v[230:231], v[74:75], v[38:39], v[230:231]
	v_pk_fma_f32 v[230:231], v[76:77], v[40:41], v[230:231]
	v_add_f32_e32 v46, v46, v230
	v_add_f32_e32 v46, v46, v231
	v_fma_f32 v47, v50, v3, v42
	v_pk_mul_f32 v[230:231], v[212:213], v[86:87]
	v_pk_fma_f32 v[230:231], v[214:215], v[30:31], v[230:231]
	v_pk_fma_f32 v[230:231], v[216:217], v[28:29], v[230:231]
	v_pk_fma_f32 v[230:231], v[218:219], v[26:27], v[230:231]
	v_pk_fma_f32 v[230:231], v[220:221], v[24:25], v[230:231]
	v_pk_fma_f32 v[230:231], v[222:223], v[22:23], v[230:231]
	v_pk_fma_f32 v[230:231], v[234:235], v[20:21], v[230:231]
	v_pk_fma_f32 v[230:231], v[236:237], v[16:17], v[230:231]
	v_pk_fma_f32 v[230:231], v[238:239], v[18:19], v[230:231]
	v_pk_fma_f32 v[230:231], v[240:241], v[32:33], v[230:231]
	v_pk_fma_f32 v[230:231], v[242:243], v[34:35], v[230:231]
	v_pk_fma_f32 v[230:231], v[244:245], v[36:37], v[230:231]
	v_pk_fma_f32 v[230:231], v[246:247], v[38:39], v[230:231]
	v_pk_fma_f32 v[230:231], v[248:249], v[40:41], v[230:231]
	v_pk_fma_f32 v[230:231], v[84:85], v[88:89], v[230:231]
	v_add_f32_e32 v47, v47, v230
	v_add_f32_e32 v47, v47, v231
	v_fma_f32 v48, v85, v88, v42
	v_fmac_f32_e32 v48, v81, v40
	v_fmac_f32_e32 v48, v84, v41
	v_pk_mul_f32 v[230:231], v[50:51], v[2:3]
	v_pk_fma_f32 v[230:231], v[52:53], v[86:87], v[230:231]
	v_pk_fma_f32 v[230:231], v[54:55], v[30:31], v[230:231]
	v_pk_fma_f32 v[230:231], v[56:57], v[28:29], v[230:231]
	v_pk_fma_f32 v[230:231], v[58:59], v[26:27], v[230:231]
	v_pk_fma_f32 v[230:231], v[60:61], v[24:25], v[230:231]
	v_pk_fma_f32 v[230:231], v[62:63], v[22:23], v[230:231]
	v_pk_fma_f32 v[230:231], v[64:65], v[20:21], v[230:231]
	v_pk_fma_f32 v[230:231], v[66:67], v[16:17], v[230:231]
	v_pk_fma_f32 v[230:231], v[68:69], v[18:19], v[230:231]
	v_pk_fma_f32 v[230:231], v[70:71], v[32:33], v[230:231]
	v_pk_fma_f32 v[230:231], v[72:73], v[34:35], v[230:231]
	v_pk_fma_f32 v[230:231], v[74:75], v[36:37], v[230:231]
	v_pk_fma_f32 v[230:231], v[76:77], v[38:39], v[230:231]
	v_add_f32_e32 v48, v48, v230
	v_add_f32_e32 v48, v48, v231
	v_fma_f32 v49, v50, v5, v42
	v_pk_mul_f32 v[230:231], v[212:213], v[2:3]
	v_pk_fma_f32 v[230:231], v[214:215], v[86:87], v[230:231]
	v_pk_fma_f32 v[230:231], v[216:217], v[30:31], v[230:231]
	v_pk_fma_f32 v[230:231], v[218:219], v[28:29], v[230:231]
	v_pk_fma_f32 v[230:231], v[220:221], v[26:27], v[230:231]
	v_pk_fma_f32 v[230:231], v[222:223], v[24:25], v[230:231]
	v_pk_fma_f32 v[230:231], v[234:235], v[22:23], v[230:231]
	v_pk_fma_f32 v[230:231], v[236:237], v[20:21], v[230:231]
	v_pk_fma_f32 v[230:231], v[238:239], v[16:17], v[230:231]
	v_pk_fma_f32 v[230:231], v[240:241], v[18:19], v[230:231]
	v_pk_fma_f32 v[230:231], v[242:243], v[32:33], v[230:231]
	v_pk_fma_f32 v[230:231], v[244:245], v[34:35], v[230:231]
	v_pk_fma_f32 v[230:231], v[246:247], v[36:37], v[230:231]
	v_pk_fma_f32 v[230:231], v[248:249], v[38:39], v[230:231]
	v_pk_fma_f32 v[230:231], v[84:85], v[40:41], v[230:231]
	v_add_f32_e32 v49, v49, v230
	v_add_f32_e32 v49, v49, v231
	v_fma_f32 v41, v85, v40, v42
	v_fmac_f32_e32 v41, v81, v38
	v_fmac_f32_e32 v41, v84, v39
	v_pk_mul_f32 v[230:231], v[50:51], v[4:5]
	v_pk_fma_f32 v[230:231], v[52:53], v[2:3], v[230:231]
	v_pk_fma_f32 v[230:231], v[54:55], v[86:87], v[230:231]
	v_pk_fma_f32 v[230:231], v[56:57], v[30:31], v[230:231]
	v_pk_fma_f32 v[230:231], v[58:59], v[28:29], v[230:231]
	v_pk_fma_f32 v[230:231], v[60:61], v[26:27], v[230:231]
	v_pk_fma_f32 v[230:231], v[62:63], v[24:25], v[230:231]
	v_pk_fma_f32 v[230:231], v[64:65], v[22:23], v[230:231]
	v_pk_fma_f32 v[230:231], v[66:67], v[20:21], v[230:231]
	v_pk_fma_f32 v[230:231], v[68:69], v[16:17], v[230:231]
	v_pk_fma_f32 v[230:231], v[70:71], v[18:19], v[230:231]
	v_pk_fma_f32 v[230:231], v[72:73], v[32:33], v[230:231]
	v_pk_fma_f32 v[230:231], v[74:75], v[34:35], v[230:231]
	v_pk_fma_f32 v[230:231], v[76:77], v[36:37], v[230:231]
	v_add_f32_e32 v41, v41, v230
	v_add_f32_e32 v41, v41, v231
	v_fma_f32 v40, v50, v7, v42
	v_pk_mul_f32 v[230:231], v[212:213], v[4:5]
	v_pk_fma_f32 v[230:231], v[214:215], v[2:3], v[230:231]
	v_pk_fma_f32 v[230:231], v[216:217], v[86:87], v[230:231]
	v_pk_fma_f32 v[230:231], v[218:219], v[30:31], v[230:231]
	v_pk_fma_f32 v[230:231], v[220:221], v[28:29], v[230:231]
	v_pk_fma_f32 v[230:231], v[222:223], v[26:27], v[230:231]
	v_pk_fma_f32 v[230:231], v[234:235], v[24:25], v[230:231]
	v_pk_fma_f32 v[230:231], v[236:237], v[22:23], v[230:231]
	v_pk_fma_f32 v[230:231], v[238:239], v[20:21], v[230:231]
	v_pk_fma_f32 v[230:231], v[240:241], v[16:17], v[230:231]
	v_pk_fma_f32 v[230:231], v[242:243], v[18:19], v[230:231]
	v_pk_fma_f32 v[230:231], v[244:245], v[32:33], v[230:231]
	v_pk_fma_f32 v[230:231], v[246:247], v[34:35], v[230:231]
	v_pk_fma_f32 v[230:231], v[248:249], v[36:37], v[230:231]
	v_pk_fma_f32 v[230:231], v[84:85], v[38:39], v[230:231]
	v_add_f32_e32 v40, v40, v230
	v_add_f32_e32 v40, v40, v231
	v_fma_f32 v39, v85, v38, v42
	v_fmac_f32_e32 v39, v81, v36
	v_fmac_f32_e32 v39, v84, v37
	v_pk_mul_f32 v[230:231], v[50:51], v[6:7]
	v_pk_fma_f32 v[230:231], v[52:53], v[4:5], v[230:231]
	v_pk_fma_f32 v[230:231], v[54:55], v[2:3], v[230:231]
	v_pk_fma_f32 v[230:231], v[56:57], v[86:87], v[230:231]
	v_pk_fma_f32 v[230:231], v[58:59], v[30:31], v[230:231]
	v_pk_fma_f32 v[230:231], v[60:61], v[28:29], v[230:231]
	v_pk_fma_f32 v[230:231], v[62:63], v[26:27], v[230:231]
	v_pk_fma_f32 v[230:231], v[64:65], v[24:25], v[230:231]
	v_pk_fma_f32 v[230:231], v[66:67], v[22:23], v[230:231]
	v_pk_fma_f32 v[230:231], v[68:69], v[20:21], v[230:231]
	v_pk_fma_f32 v[230:231], v[70:71], v[16:17], v[230:231]
	v_pk_fma_f32 v[230:231], v[72:73], v[18:19], v[230:231]
	v_pk_fma_f32 v[230:231], v[74:75], v[32:33], v[230:231]
	v_pk_fma_f32 v[230:231], v[76:77], v[34:35], v[230:231]
	v_add_f32_e32 v39, v39, v230
	v_add_f32_e32 v39, v39, v231
	v_fma_f32 v38, v50, v9, v42
	v_pk_mul_f32 v[230:231], v[212:213], v[6:7]
	v_pk_fma_f32 v[230:231], v[214:215], v[4:5], v[230:231]
	v_pk_fma_f32 v[230:231], v[216:217], v[2:3], v[230:231]
	v_pk_fma_f32 v[230:231], v[218:219], v[86:87], v[230:231]
	v_pk_fma_f32 v[230:231], v[220:221], v[30:31], v[230:231]
	v_pk_fma_f32 v[230:231], v[222:223], v[28:29], v[230:231]
	v_pk_fma_f32 v[230:231], v[234:235], v[26:27], v[230:231]
	v_pk_fma_f32 v[230:231], v[236:237], v[24:25], v[230:231]
	v_pk_fma_f32 v[230:231], v[238:239], v[22:23], v[230:231]
	v_pk_fma_f32 v[230:231], v[240:241], v[20:21], v[230:231]
	v_pk_fma_f32 v[230:231], v[242:243], v[16:17], v[230:231]
	v_pk_fma_f32 v[230:231], v[244:245], v[18:19], v[230:231]
	v_pk_fma_f32 v[230:231], v[246:247], v[32:33], v[230:231]
	v_pk_fma_f32 v[230:231], v[248:249], v[34:35], v[230:231]
	v_pk_fma_f32 v[230:231], v[84:85], v[36:37], v[230:231]
	v_add_f32_e32 v38, v38, v230
	v_add_f32_e32 v38, v38, v231
	v_fma_f32 v37, v85, v36, v42
	v_fmac_f32_e32 v37, v81, v34
	v_fmac_f32_e32 v37, v84, v35
	v_pk_mul_f32 v[230:231], v[50:51], v[8:9]
	v_pk_fma_f32 v[230:231], v[52:53], v[6:7], v[230:231]
	v_pk_fma_f32 v[230:231], v[54:55], v[4:5], v[230:231]
	v_pk_fma_f32 v[230:231], v[56:57], v[2:3], v[230:231]
	v_pk_fma_f32 v[230:231], v[58:59], v[86:87], v[230:231]
	v_pk_fma_f32 v[230:231], v[60:61], v[30:31], v[230:231]
	v_pk_fma_f32 v[230:231], v[62:63], v[28:29], v[230:231]
	v_pk_fma_f32 v[230:231], v[64:65], v[26:27], v[230:231]
	v_pk_fma_f32 v[230:231], v[66:67], v[24:25], v[230:231]
	v_pk_fma_f32 v[230:231], v[68:69], v[22:23], v[230:231]
	v_pk_fma_f32 v[230:231], v[70:71], v[20:21], v[230:231]
	v_pk_fma_f32 v[230:231], v[72:73], v[16:17], v[230:231]
	v_pk_fma_f32 v[230:231], v[74:75], v[18:19], v[230:231]
	v_pk_fma_f32 v[230:231], v[76:77], v[32:33], v[230:231]
	v_add_f32_e32 v37, v37, v230
	v_add_f32_e32 v37, v37, v231
	v_fma_f32 v36, v50, v11, v42
	v_pk_mul_f32 v[230:231], v[212:213], v[8:9]
	v_pk_fma_f32 v[230:231], v[214:215], v[6:7], v[230:231]
	v_pk_fma_f32 v[230:231], v[216:217], v[4:5], v[230:231]
	v_pk_fma_f32 v[230:231], v[218:219], v[2:3], v[230:231]
	v_pk_fma_f32 v[230:231], v[220:221], v[86:87], v[230:231]
	v_pk_fma_f32 v[230:231], v[222:223], v[30:31], v[230:231]
	v_pk_fma_f32 v[230:231], v[234:235], v[28:29], v[230:231]
	v_pk_fma_f32 v[230:231], v[236:237], v[26:27], v[230:231]
	v_pk_fma_f32 v[230:231], v[238:239], v[24:25], v[230:231]
	v_pk_fma_f32 v[230:231], v[240:241], v[22:23], v[230:231]
	v_pk_fma_f32 v[230:231], v[242:243], v[20:21], v[230:231]
	v_pk_fma_f32 v[230:231], v[244:245], v[16:17], v[230:231]
	v_pk_fma_f32 v[230:231], v[246:247], v[18:19], v[230:231]
	v_pk_fma_f32 v[230:231], v[248:249], v[32:33], v[230:231]
	v_pk_fma_f32 v[230:231], v[84:85], v[34:35], v[230:231]
	v_add_f32_e32 v36, v36, v230
	v_add_f32_e32 v36, v36, v231
	v_fma_f32 v35, v85, v34, v42
	v_fmac_f32_e32 v35, v81, v32
	v_fmac_f32_e32 v35, v84, v33
	v_pk_mul_f32 v[230:231], v[50:51], v[10:11]
	v_pk_fma_f32 v[230:231], v[52:53], v[8:9], v[230:231]
	v_pk_fma_f32 v[230:231], v[54:55], v[6:7], v[230:231]
	v_pk_fma_f32 v[230:231], v[56:57], v[4:5], v[230:231]
	v_pk_fma_f32 v[230:231], v[58:59], v[2:3], v[230:231]
	v_pk_fma_f32 v[230:231], v[60:61], v[86:87], v[230:231]
	v_pk_fma_f32 v[230:231], v[62:63], v[30:31], v[230:231]
	v_pk_fma_f32 v[230:231], v[64:65], v[28:29], v[230:231]
	v_pk_fma_f32 v[230:231], v[66:67], v[26:27], v[230:231]
	v_pk_fma_f32 v[230:231], v[68:69], v[24:25], v[230:231]
	v_pk_fma_f32 v[230:231], v[70:71], v[22:23], v[230:231]
	v_pk_fma_f32 v[230:231], v[72:73], v[20:21], v[230:231]
	v_pk_fma_f32 v[230:231], v[74:75], v[16:17], v[230:231]
	v_pk_fma_f32 v[230:231], v[76:77], v[18:19], v[230:231]
	v_add_f32_e32 v35, v35, v230
	v_add_f32_e32 v35, v35, v231
	v_fma_f32 v34, v50, v13, v42
	v_pk_mul_f32 v[230:231], v[212:213], v[10:11]
	v_pk_fma_f32 v[230:231], v[214:215], v[8:9], v[230:231]
	v_pk_fma_f32 v[230:231], v[216:217], v[6:7], v[230:231]
	v_pk_fma_f32 v[230:231], v[218:219], v[4:5], v[230:231]
	v_pk_fma_f32 v[230:231], v[220:221], v[2:3], v[230:231]
	v_pk_fma_f32 v[230:231], v[222:223], v[86:87], v[230:231]
	v_pk_fma_f32 v[230:231], v[234:235], v[30:31], v[230:231]
	v_pk_fma_f32 v[230:231], v[236:237], v[28:29], v[230:231]
	v_pk_fma_f32 v[230:231], v[238:239], v[26:27], v[230:231]
	v_pk_fma_f32 v[230:231], v[240:241], v[24:25], v[230:231]
	v_pk_fma_f32 v[230:231], v[242:243], v[22:23], v[230:231]
	v_pk_fma_f32 v[230:231], v[244:245], v[20:21], v[230:231]
	v_pk_fma_f32 v[230:231], v[246:247], v[16:17], v[230:231]
	v_pk_fma_f32 v[230:231], v[248:249], v[18:19], v[230:231]
	v_pk_fma_f32 v[230:231], v[84:85], v[32:33], v[230:231]
	v_add_f32_e32 v34, v34, v230
	v_add_f32_e32 v34, v34, v231
	v_fma_f32 v33, v85, v32, v42
	v_fmac_f32_e32 v33, v81, v18
	v_fmac_f32_e32 v33, v84, v19
	v_pk_mul_f32 v[230:231], v[50:51], v[12:13]
	v_pk_fma_f32 v[230:231], v[52:53], v[10:11], v[230:231]
	v_pk_fma_f32 v[230:231], v[54:55], v[8:9], v[230:231]
	v_pk_fma_f32 v[230:231], v[56:57], v[6:7], v[230:231]
	v_pk_fma_f32 v[230:231], v[58:59], v[4:5], v[230:231]
	v_pk_fma_f32 v[230:231], v[60:61], v[2:3], v[230:231]
	v_pk_fma_f32 v[230:231], v[62:63], v[86:87], v[230:231]
	v_pk_fma_f32 v[230:231], v[64:65], v[30:31], v[230:231]
	v_pk_fma_f32 v[230:231], v[66:67], v[28:29], v[230:231]
	v_pk_fma_f32 v[230:231], v[68:69], v[26:27], v[230:231]
	v_pk_fma_f32 v[230:231], v[70:71], v[24:25], v[230:231]
	v_pk_fma_f32 v[230:231], v[72:73], v[22:23], v[230:231]
	v_pk_fma_f32 v[230:231], v[74:75], v[20:21], v[230:231]
	v_pk_fma_f32 v[230:231], v[76:77], v[16:17], v[230:231]
	v_add_f32_e32 v33, v33, v230
	v_add_f32_e32 v33, v33, v231
	v_fma_f32 v32, v50, v15, v42
	v_pk_mul_f32 v[230:231], v[212:213], v[12:13]
	v_pk_fma_f32 v[230:231], v[214:215], v[10:11], v[230:231]
	v_pk_fma_f32 v[230:231], v[216:217], v[8:9], v[230:231]
	v_pk_fma_f32 v[230:231], v[218:219], v[6:7], v[230:231]
	v_pk_fma_f32 v[230:231], v[220:221], v[4:5], v[230:231]
	v_pk_fma_f32 v[230:231], v[222:223], v[2:3], v[230:231]
	v_pk_fma_f32 v[230:231], v[234:235], v[86:87], v[230:231]
	v_pk_fma_f32 v[230:231], v[236:237], v[30:31], v[230:231]
	v_pk_fma_f32 v[230:231], v[238:239], v[28:29], v[230:231]
	v_pk_fma_f32 v[230:231], v[240:241], v[26:27], v[230:231]
	v_pk_fma_f32 v[230:231], v[242:243], v[24:25], v[230:231]
	v_pk_fma_f32 v[230:231], v[244:245], v[22:23], v[230:231]
	v_pk_fma_f32 v[230:231], v[246:247], v[20:21], v[230:231]
	v_pk_fma_f32 v[230:231], v[248:249], v[16:17], v[230:231]
	v_pk_fma_f32 v[230:231], v[84:85], v[18:19], v[230:231]
	v_add_f32_e32 v32, v32, v230
	v_add_f32_e32 v32, v32, v231
	v_fma_f32 v42, v85, v18, v42
	v_fmac_f32_e32 v42, v81, v16
	v_fmac_f32_e32 v42, v84, v17
	v_pk_mul_f32 v[230:231], v[50:51], v[14:15]
	v_pk_fma_f32 v[230:231], v[52:53], v[12:13], v[230:231]
	v_pk_fma_f32 v[230:231], v[54:55], v[10:11], v[230:231]
	v_pk_fma_f32 v[230:231], v[56:57], v[8:9], v[230:231]
	v_pk_fma_f32 v[230:231], v[58:59], v[6:7], v[230:231]
	v_pk_fma_f32 v[230:231], v[60:61], v[4:5], v[230:231]
	v_pk_fma_f32 v[230:231], v[62:63], v[2:3], v[230:231]
	v_pk_fma_f32 v[230:231], v[64:65], v[86:87], v[230:231]
	v_pk_fma_f32 v[230:231], v[66:67], v[30:31], v[230:231]
	v_pk_fma_f32 v[230:231], v[68:69], v[28:29], v[230:231]
	v_pk_fma_f32 v[230:231], v[70:71], v[26:27], v[230:231]
	v_pk_fma_f32 v[230:231], v[72:73], v[24:25], v[230:231]
	v_pk_fma_f32 v[230:231], v[74:75], v[22:23], v[230:231]
	v_pk_fma_f32 v[230:231], v[76:77], v[20:21], v[230:231]
	v_add_f32_e32 v42, v42, v230
	v_add_f32_e32 v42, v42, v231
	v_lshl_add_u64 v[26:27], v[82:83], 1, s[16:17]
	v_or_b32_e32 v30, 0x1000, v114
	v_mov_b32_e32 v31, v115
	v_lshl_add_u64 v[28:29], v[26:27], 0, v[114:115]
	v_lshl_add_u64 v[14:15], v[26:27], 0, v[30:31]
	global_load_dwordx4 v[6:9], v[28:29], off
	v_or_b32_e32 v2, s2, v91
	global_load_dwordx4 v[14:17], v[14:15], off
	v_mul_u32_u24_e32 v2, 0x210, v2
	v_add3_u32 v22, s3, v2, v92
	ds_read_b128 v[2:5], v22
	v_or_b32_e32 v114, 0x1800, v114
	s_waitcnt vmcnt(0) lgkmcnt(0)
	v_mfma_f32_16x16x32_bf16 v[18:21], v[14:17], v[2:5], 0
	v_lshl_add_u64 v[14:15], v[26:27], 0, v[114:115]
	global_load_dwordx4 v[10:13], v[28:29], off offset:2048
	ds_read_b128 v[22:25], v22 offset:64
	global_load_dwordx4 v[14:17], v[14:15], off
	v_mfma_f32_16x16x32_bf16 v[6:9], v[6:9], v[2:5], 0
	v_lshl_add_u64 v[26:27], v[26:27], 0, 64
	s_lshl_b64 s[16:17], s[0:1], 2
	s_add_u32 s16, s30, s16
	s_waitcnt vmcnt(1)
	v_mfma_f32_16x16x32_bf16 v[10:13], v[10:13], v[2:5], 0
	s_addc_u32 s17, s27, s17
	s_waitcnt vmcnt(0)
	v_mfma_f32_16x16x32_bf16 v[2:5], v[14:17], v[2:5], 0
	global_load_dwordx4 v[14:17], v[28:29], off offset:64
	v_readlane_b32 s44, v251, 28
	s_waitcnt vmcnt(0) lgkmcnt(0)
	v_mfma_f32_16x16x32_bf16 v[14:17], v[14:17], v[22:25], v[6:9]
	s_nop 2
	global_load_dwordx4 v[6:9], v[28:29], off offset:2112
	v_readlane_b32 s45, v251, 29
	v_readlane_b32 s46, v251, 30
	s_waitcnt vmcnt(0)
	v_mfma_f32_16x16x32_bf16 v[10:13], v[6:9], v[22:25], v[10:13]
	v_lshl_add_u64 v[6:7], v[26:27], 0, v[30:31]
	global_load_dwordx4 v[6:9], v[6:7], off
	v_readlane_b32 s47, v251, 31
	s_waitcnt vmcnt(0)
	v_mfma_f32_16x16x32_bf16 v[6:9], v[6:9], v[22:25], v[18:21]
	s_nop 2
	v_lshl_add_u64 v[18:19], v[26:27], 0, v[114:115]
	global_load_dwordx4 v[18:21], v[18:19], off
	v_readlane_b32 s48, v251, 32
	s_waitcnt vmcnt(0)
	v_mfma_f32_16x16x32_bf16 v[2:5], v[18:21], v[22:25], v[2:5]
	v_or_b32_e32 v18, s2, v80
	v_ashrrev_i32_e32 v19, 31, v18
	v_lshlrev_b64 v[18:19], 11, v[18:19]
	v_lshl_add_u64 v[18:19], s[86:87], 0, v[18:19]
	v_lshl_add_u64 v[22:23], v[78:79], 2, s[16:17]
	v_lshl_add_u64 v[24:25], s[0:1], 1, v[18:19]
	global_load_dwordx4 v[18:21], v[22:23], off
	s_lshl_b32 s0, s91, 2
	s_add_i32 s2, s0, s90
	s_ashr_i32 s3, s2, 31
	s_lshl_b64 s[2:3], s[2:3], 11
	s_add_u32 s2, s86, s2
	s_addc_u32 s3, s87, s3
	v_readlane_b32 s49, v251, 33
	v_readlane_b32 s50, v251, 34
	v_readlane_b32 s51, v251, 35
	s_waitcnt vmcnt(0)
	v_pk_mul_f32 v[14:15], v[14:15], v[18:19]
	v_pk_mul_f32 v[16:17], v[16:17], v[20:21]
	v_cvt_pk_bf16_f32 v14, v14, v15
	v_cvt_pk_bf16_f32 v15, v16, v17
	v_lshl_add_u64 v[18:19], v[78:79], 1, v[24:25]
	global_store_dwordx2 v[18:19], v[14:15], off offset:512
	global_load_dwordx4 v[14:17], v[22:23], off offset:64
	s_waitcnt vmcnt(0)
	v_pk_mul_f32 v[10:11], v[10:11], v[14:15]
	v_pk_mul_f32 v[12:13], v[12:13], v[16:17]
	v_cvt_pk_bf16_f32 v10, v10, v11
	v_cvt_pk_bf16_f32 v11, v12, v13
	global_store_dwordx2 v[18:19], v[10:11], off offset:544
	global_load_dwordx4 v[10:13], v[22:23], off offset:128
	s_waitcnt vmcnt(0)
	v_pk_mul_f32 v[6:7], v[6:7], v[10:11]
	v_pk_mul_f32 v[8:9], v[8:9], v[12:13]
	v_cvt_pk_bf16_f32 v6, v6, v7
	v_cvt_pk_bf16_f32 v7, v8, v9
	global_store_dwordx2 v[18:19], v[6:7], off offset:576
	global_load_dwordx4 v[6:9], v[22:23], off offset:192
	v_mov_b32_e32 v13, v115
	v_mov_b32_e32 v22, 0x3b800000
	s_waitcnt vmcnt(0)
	v_pk_mul_f32 v[2:3], v[2:3], v[6:7]
	v_pk_mul_f32 v[4:5], v[4:5], v[8:9]
	v_cvt_pk_bf16_f32 v2, v2, v3
	v_cvt_pk_bf16_f32 v3, v4, v5
	global_store_dwordx2 v[18:19], v[2:3], off offset:608
	v_add_u32_e32 v2, 0, v43
	v_lshlrev_b32_e32 v6, 2, v1
	v_lshl_add_u32 v1, v1, 4, 0
	ds_write2st64_b32 v2, v42, v32 offset1:4
	ds_write2st64_b32 v2, v33, v34 offset0:8 offset1:12
	ds_write2st64_b32 v2, v35, v36 offset0:16 offset1:20
	ds_write2st64_b32 v2, v37, v38 offset0:24 offset1:28
	ds_write2st64_b32 v2, v39, v40 offset0:32 offset1:36
	ds_write2st64_b32 v2, v41, v49 offset0:40 offset1:44
	ds_write2st64_b32 v2, v48, v47 offset0:48 offset1:52
	ds_write_b32 v2, v46 offset:14336
	v_add_u32_e32 v2, 0, v44
	v_lshl_add_u32 v8, s91, 12, v1
	ds_write_b32 v2, v45
	s_waitcnt lgkmcnt(0)
	s_barrier
	ds_read_b128 v[8:11], v8
	v_ashrrev_i32_e32 v7, 31, v6
	v_lshlrev_b64 v[2:3], 2, v[6:7]
	v_lshl_add_u64 v[4:5], s[76:77], 0, v[2:3]
	v_lshl_add_u64 v[2:3], s[14:15], 0, v[2:3]
	s_waitcnt lgkmcnt(0)
	v_add_f32_e32 v12, v8, v9
	v_add_f32_e32 v12, v10, v12
	v_add_f32_e32 v12, v11, v12
	v_lshlrev_b64 v[6:7], 1, v[6:7]
	s_nop 0
	v_add_f32_dpp v12, v12, v12 quad_perm:[1,0,3,2] row_mask:0xf bank_mask:0xf bound_ctrl:1
	s_nop 1
	v_add_f32_dpp v12, v12, v12 quad_perm:[2,3,0,1] row_mask:0xf bank_mask:0xf bound_ctrl:1
	s_nop 1
	v_add_f32_dpp v12, v12, v12 row_half_mirror row_mask:0xf bank_mask:0xf bound_ctrl:1
	s_nop 1
	v_add_f32_dpp v12, v12, v12 row_mirror row_mask:0xf bank_mask:0xf bound_ctrl:1
	s_nop 1
	v_mov_b32_dpp v13, v12 row_bcast:15 row_mask:0xa bank_mask:0xf
	v_add_f32_e32 v12, v12, v13
	v_mov_b32_e32 v13, v115
	s_nop 1
	v_mov_b32_dpp v13, v12 row_bcast:31 row_mask:0xc bank_mask:0xf
	v_add_f32_e32 v12, v12, v13
	s_nop 0
	v_readlane_b32 s1, v12, 63
	s_nop 1
	v_fmac_f32_e32 v9, s1, v250
	v_fma_f32 v17, s1, v250, v11
	v_fma_f32 v16, s1, v250, v10
	v_fma_f32 v8, s1, v250, v8
	v_mul_f32_e32 v12, v9, v9
	v_fmac_f32_e32 v12, v8, v8
	v_pk_mul_f32 v[10:11], v[16:17], v[16:17]
	s_nop 0
	v_add_f32_e32 v10, v10, v12
	v_add_f32_e32 v10, v11, v10
	v_mov_b32_e32 v11, v115
	s_nop 0
	v_add_f32_dpp v10, v10, v10 quad_perm:[1,0,3,2] row_mask:0xf bank_mask:0xf bound_ctrl:1
	s_nop 1
	v_add_f32_dpp v10, v10, v10 quad_perm:[2,3,0,1] row_mask:0xf bank_mask:0xf bound_ctrl:1
	s_nop 1
	v_add_f32_dpp v10, v10, v10 row_half_mirror row_mask:0xf bank_mask:0xf bound_ctrl:1
	s_nop 1
	v_add_f32_dpp v10, v10, v10 row_mirror row_mask:0xf bank_mask:0xf bound_ctrl:1
	s_nop 1
	v_mov_b32_dpp v11, v10 row_bcast:15 row_mask:0xa bank_mask:0xf
	v_add_f32_e32 v10, v10, v11
	v_mov_b32_e32 v11, v115
	s_nop 1
	v_mov_b32_dpp v11, v10 row_bcast:31 row_mask:0xc bank_mask:0xf
	v_add_f32_e32 v10, v10, v11
	s_nop 0
	v_readlane_b32 s1, v10, 63
	s_nop 1
	v_fma_f32 v10, s1, v22, v225
	v_rsq_f32_e32 v18, v10
	s_or_b32 s1, s0, 1
	v_pk_mul_f32 v[20:21], v[8:9], v[18:19] op_sel_hi:[1,0]
	global_load_dwordx4 v[8:11], v[4:5], off
	global_load_dwordx4 v[12:15], v[2:3], off
	s_waitcnt vmcnt(0)
	v_pk_fma_f32 v[8:9], v[8:9], v[20:21], v[12:13]
	s_nop 0
	v_mul_f32_e32 v12, 0xbfb8aa3b, v8
	v_mul_f32_e32 v13, 0xbfb8aa3b, v9
	v_exp_f32_e32 v12, v12
	v_exp_f32_e32 v13, v13
	v_add_f32_e32 v12, 1.0, v12
	v_add_f32_e32 v13, 1.0, v13
	v_rcp_f32_e32 v12, v12
	v_rcp_f32_e32 v13, v13
	s_nop 0
	v_pk_mul_f32 v[8:9], v[8:9], v[12:13]
	v_pk_mul_f32 v[12:13], v[16:17], v[18:19] op_sel_hi:[1,0]
	v_cvt_pk_bf16_f32 v8, v8, v9
	v_pk_fma_f32 v[10:11], v[12:13], v[10:11], v[14:15]
	s_nop 0
	v_mul_f32_e32 v12, 0xbfb8aa3b, v10
	v_mul_f32_e32 v13, 0xbfb8aa3b, v11
	v_exp_f32_e32 v12, v12
	v_exp_f32_e32 v13, v13
	v_add_f32_e32 v12, 1.0, v12
	v_add_f32_e32 v13, 1.0, v13
	v_rcp_f32_e32 v12, v12
	v_rcp_f32_e32 v13, v13
	s_nop 0
	v_pk_mul_f32 v[10:11], v[10:11], v[12:13]
	s_nop 0
	v_cvt_pk_bf16_f32 v9, v10, v11
	v_lshl_add_u64 v[10:11], s[2:3], 0, v[6:7]
	global_store_dwordx2 v[10:11], v[8:9], off offset:1536
	v_lshl_add_u32 v8, s1, 10, v1
	ds_read_b128 v[12:15], v8
	v_mov_b32_e32 v9, v115
	s_waitcnt lgkmcnt(0)
	v_add_f32_e32 v8, v12, v13
	v_add_f32_e32 v8, v14, v8
	v_add_f32_e32 v8, v15, v8
	s_nop 1
	v_add_f32_dpp v8, v8, v8 quad_perm:[1,0,3,2] row_mask:0xf bank_mask:0xf bound_ctrl:1
	s_nop 1
	v_add_f32_dpp v8, v8, v8 quad_perm:[2,3,0,1] row_mask:0xf bank_mask:0xf bound_ctrl:1
	s_nop 1
	v_add_f32_dpp v8, v8, v8 row_half_mirror row_mask:0xf bank_mask:0xf bound_ctrl:1
	s_nop 1
	v_add_f32_dpp v8, v8, v8 row_mirror row_mask:0xf bank_mask:0xf bound_ctrl:1
	s_nop 1
	v_mov_b32_dpp v9, v8 row_bcast:15 row_mask:0xa bank_mask:0xf
	v_add_f32_e32 v8, v8, v9
	v_mov_b32_e32 v9, v115
	s_nop 1
	v_mov_b32_dpp v9, v8 row_bcast:31 row_mask:0xc bank_mask:0xf
	v_add_f32_e32 v8, v8, v9
	s_nop 0
	v_readlane_b32 s2, v8, 63
	s_nop 1
	v_fmac_f32_e32 v13, s2, v250
	v_fma_f32 v9, s2, v250, v15
	v_fma_f32 v8, s2, v250, v14
	v_fma_f32 v12, s2, v250, v12
	v_mul_f32_e32 v14, v13, v13
	v_fmac_f32_e32 v14, v12, v12
	v_pk_mul_f32 v[10:11], v[8:9], v[8:9]
	s_nop 0
	v_add_f32_e32 v10, v10, v14
	global_load_dwordx4 v[14:17], v[4:5], off
	global_load_dwordx4 v[18:21], v[2:3], off
	v_add_f32_e32 v10, v11, v10
	v_mov_b32_e32 v11, v115
	s_nop 0
	v_add_f32_dpp v10, v10, v10 quad_perm:[1,0,3,2] row_mask:0xf bank_mask:0xf bound_ctrl:1
	s_nop 1
	v_add_f32_dpp v10, v10, v10 quad_perm:[2,3,0,1] row_mask:0xf bank_mask:0xf bound_ctrl:1
	s_nop 1
	v_add_f32_dpp v10, v10, v10 row_half_mirror row_mask:0xf bank_mask:0xf bound_ctrl:1
	s_nop 1
	v_add_f32_dpp v10, v10, v10 row_mirror row_mask:0xf bank_mask:0xf bound_ctrl:1
	s_nop 1
	v_mov_b32_dpp v11, v10 row_bcast:15 row_mask:0xa bank_mask:0xf
	v_add_f32_e32 v10, v10, v11
	v_mov_b32_e32 v11, v115
	s_nop 1
	v_mov_b32_dpp v11, v10 row_bcast:31 row_mask:0xc bank_mask:0xf
	v_add_f32_e32 v10, v10, v11
	s_nop 0
	v_readlane_b32 s2, v10, 63
	s_nop 1
	v_fma_f32 v10, s2, v22, v225
	v_rsq_f32_e32 v10, v10
	s_add_i32 s2, s1, s90
	s_ashr_i32 s3, s2, 31
	s_lshl_b64 s[2:3], s[2:3], 11
	v_pk_mul_f32 v[12:13], v[12:13], v[10:11] op_sel_hi:[1,0]
	s_add_u32 s2, s86, s2
	s_addc_u32 s3, s87, s3
	s_or_b32 s1, s0, 2
	s_waitcnt vmcnt(0)
	v_pk_fma_f32 v[12:13], v[14:15], v[12:13], v[18:19]
	s_nop 0
	v_mul_f32_e32 v11, 0xbfb8aa3b, v12
	v_exp_f32_e32 v11, v11
	s_nop 0
	v_add_f32_e32 v11, 1.0, v11
	v_rcp_f32_e32 v14, v11
	v_mul_f32_e32 v11, 0xbfb8aa3b, v13
	v_exp_f32_e32 v11, v11
	s_nop 0
	v_add_f32_e32 v11, 1.0, v11
	v_pk_mul_f32 v[8:9], v[8:9], v[10:11] op_sel_hi:[1,0]
	v_rcp_f32_e32 v15, v11
	v_pk_fma_f32 v[8:9], v[8:9], v[16:17], v[20:21]
	v_pk_mul_f32 v[12:13], v[12:13], v[14:15]
	v_mul_f32_e32 v10, 0xbfb8aa3b, v8
	v_mul_f32_e32 v11, 0xbfb8aa3b, v9
	v_exp_f32_e32 v10, v10
	v_exp_f32_e32 v11, v11
	v_add_f32_e32 v10, 1.0, v10
	v_add_f32_e32 v11, 1.0, v11
	v_rcp_f32_e32 v10, v10
	v_rcp_f32_e32 v11, v11
	s_nop 0
	v_pk_mul_f32 v[8:9], v[8:9], v[10:11]
	v_cvt_pk_bf16_f32 v10, v12, v13
	v_cvt_pk_bf16_f32 v11, v8, v9
	v_lshl_add_u64 v[8:9], s[2:3], 0, v[6:7]
	global_store_dwordx2 v[8:9], v[10:11], off offset:1536
	v_lshl_add_u32 v8, s1, 10, v1
	ds_read_b128 v[8:11], v8
	v_mov_b32_e32 v13, v115
	s_waitcnt lgkmcnt(0)
	v_add_f32_e32 v12, v8, v9
	v_add_f32_e32 v12, v10, v12
	v_add_f32_e32 v12, v11, v12
	s_nop 1
	v_add_f32_dpp v12, v12, v12 quad_perm:[1,0,3,2] row_mask:0xf bank_mask:0xf bound_ctrl:1
	s_nop 1
	v_add_f32_dpp v12, v12, v12 quad_perm:[2,3,0,1] row_mask:0xf bank_mask:0xf bound_ctrl:1
	s_nop 1
	v_add_f32_dpp v12, v12, v12 row_half_mirror row_mask:0xf bank_mask:0xf bound_ctrl:1
	s_nop 1
	v_add_f32_dpp v12, v12, v12 row_mirror row_mask:0xf bank_mask:0xf bound_ctrl:1
	s_nop 1
	v_mov_b32_dpp v13, v12 row_bcast:15 row_mask:0xa bank_mask:0xf
	v_add_f32_e32 v12, v12, v13
	v_mov_b32_e32 v13, v115
	s_nop 1
	v_mov_b32_dpp v13, v12 row_bcast:31 row_mask:0xc bank_mask:0xf
	v_add_f32_e32 v12, v12, v13
	s_nop 0
	v_readlane_b32 s2, v12, 63
	s_nop 1
	v_fmac_f32_e32 v9, s2, v250
	v_fma_f32 v17, s2, v250, v11
	v_fma_f32 v16, s2, v250, v10
	v_fma_f32 v8, s2, v250, v8
	v_mul_f32_e32 v12, v9, v9
	v_fmac_f32_e32 v12, v8, v8
	v_pk_mul_f32 v[10:11], v[16:17], v[16:17]
	s_nop 0
	v_add_f32_e32 v10, v10, v12
	v_add_f32_e32 v10, v11, v10
	v_mov_b32_e32 v11, v115
	s_nop 0
	v_add_f32_dpp v10, v10, v10 quad_perm:[1,0,3,2] row_mask:0xf bank_mask:0xf bound_ctrl:1
	s_nop 1
	v_add_f32_dpp v10, v10, v10 quad_perm:[2,3,0,1] row_mask:0xf bank_mask:0xf bound_ctrl:1
	s_nop 1
	v_add_f32_dpp v10, v10, v10 row_half_mirror row_mask:0xf bank_mask:0xf bound_ctrl:1
	s_nop 1
	v_add_f32_dpp v10, v10, v10 row_mirror row_mask:0xf bank_mask:0xf bound_ctrl:1
	s_nop 1
	v_mov_b32_dpp v11, v10 row_bcast:15 row_mask:0xa bank_mask:0xf
	v_add_f32_e32 v10, v10, v11
	v_mov_b32_e32 v11, v115
	s_nop 1
	v_mov_b32_dpp v11, v10 row_bcast:31 row_mask:0xc bank_mask:0xf
	v_add_f32_e32 v10, v10, v11
	s_nop 0
	v_readlane_b32 s2, v10, 63
	s_nop 1
	v_fma_f32 v10, s2, v22, v225
	v_rsq_f32_e32 v18, v10
	s_add_i32 s2, s1, s90
	s_ashr_i32 s3, s2, 31
	s_lshl_b64 s[2:3], s[2:3], 11
	v_pk_mul_f32 v[20:21], v[8:9], v[18:19] op_sel_hi:[1,0]
	global_load_dwordx4 v[8:11], v[4:5], off
	global_load_dwordx4 v[12:15], v[2:3], off
	s_add_u32 s2, s86, s2
	s_addc_u32 s3, s87, s3
	s_or_b32 s0, s0, 3
	v_lshl_add_u32 v1, s0, 10, v1
	s_add_i32 s0, s0, s90
	s_waitcnt vmcnt(0)
	v_pk_fma_f32 v[8:9], v[8:9], v[20:21], v[12:13]
	s_nop 0
	v_mul_f32_e32 v12, 0xbfb8aa3b, v8
	v_mul_f32_e32 v13, 0xbfb8aa3b, v9
	v_exp_f32_e32 v12, v12
	v_exp_f32_e32 v13, v13
	v_add_f32_e32 v12, 1.0, v12
	v_add_f32_e32 v13, 1.0, v13
	v_rcp_f32_e32 v12, v12
	v_rcp_f32_e32 v13, v13
	s_nop 0
	v_pk_mul_f32 v[8:9], v[8:9], v[12:13]
	v_pk_mul_f32 v[12:13], v[16:17], v[18:19] op_sel_hi:[1,0]
	v_cvt_pk_bf16_f32 v8, v8, v9
	v_pk_fma_f32 v[10:11], v[12:13], v[10:11], v[14:15]
	s_nop 0
	v_mul_f32_e32 v12, 0xbfb8aa3b, v10
	v_mul_f32_e32 v13, 0xbfb8aa3b, v11
	v_exp_f32_e32 v12, v12
	v_exp_f32_e32 v13, v13
	v_add_f32_e32 v12, 1.0, v12
	v_add_f32_e32 v13, 1.0, v13
	v_rcp_f32_e32 v12, v12
	v_rcp_f32_e32 v13, v13
	s_nop 0
	v_pk_mul_f32 v[10:11], v[10:11], v[12:13]
	ds_read_b128 v[12:15], v1
	v_cvt_pk_bf16_f32 v9, v10, v11
	v_lshl_add_u64 v[10:11], s[2:3], 0, v[6:7]
	global_store_dwordx2 v[10:11], v[8:9], off offset:1536
	v_mov_b32_e32 v8, v115
	s_waitcnt lgkmcnt(0)
	v_add_f32_e32 v1, v12, v13
	v_add_f32_e32 v1, v14, v1
	v_add_f32_e32 v1, v15, v1
	s_nop 1
	v_add_f32_dpp v1, v1, v1 quad_perm:[1,0,3,2] row_mask:0xf bank_mask:0xf bound_ctrl:1
	s_nop 1
	v_add_f32_dpp v1, v1, v1 quad_perm:[2,3,0,1] row_mask:0xf bank_mask:0xf bound_ctrl:1
	s_nop 1
	v_add_f32_dpp v1, v1, v1 row_half_mirror row_mask:0xf bank_mask:0xf bound_ctrl:1
	s_nop 1
	v_add_f32_dpp v1, v1, v1 row_mirror row_mask:0xf bank_mask:0xf bound_ctrl:1
	s_nop 1
	v_mov_b32_dpp v8, v1 row_bcast:15 row_mask:0xa bank_mask:0xf
	v_add_f32_e32 v1, v1, v8
	v_mov_b32_e32 v8, v115
	s_nop 1
	v_mov_b32_dpp v8, v1 row_bcast:31 row_mask:0xc bank_mask:0xf
	v_add_f32_e32 v1, v1, v8
	s_nop 0
	v_readlane_b32 s1, v1, 63
	s_nop 1
	v_fma_f32 v9, s1, v250, v15
	v_fma_f32 v8, s1, v250, v14
	global_load_dwordx4 v[14:17], v[4:5], off
	s_nop 0
	global_load_dwordx4 v[2:5], v[2:3], off
	v_fmac_f32_e32 v13, s1, v250
	v_fma_f32 v12, s1, v250, v12
	v_mul_f32_e32 v1, v13, v13
	v_fmac_f32_e32 v1, v12, v12
	v_pk_mul_f32 v[10:11], v[8:9], v[8:9]
	s_nop 0
	v_add_f32_e32 v1, v10, v1
	v_add_f32_e32 v1, v11, v1
	v_mov_b32_e32 v10, v115
	s_nop 0
	v_add_f32_dpp v1, v1, v1 quad_perm:[1,0,3,2] row_mask:0xf bank_mask:0xf bound_ctrl:1
	s_nop 1
	v_add_f32_dpp v1, v1, v1 quad_perm:[2,3,0,1] row_mask:0xf bank_mask:0xf bound_ctrl:1
	s_nop 1
	v_add_f32_dpp v1, v1, v1 row_half_mirror row_mask:0xf bank_mask:0xf bound_ctrl:1
	s_nop 1
	v_add_f32_dpp v1, v1, v1 row_mirror row_mask:0xf bank_mask:0xf bound_ctrl:1
	s_nop 1
	v_mov_b32_dpp v10, v1 row_bcast:15 row_mask:0xa bank_mask:0xf
	v_add_f32_e32 v1, v1, v10
	v_mov_b32_e32 v10, v115
	s_nop 1
	v_mov_b32_dpp v10, v1 row_bcast:31 row_mask:0xc bank_mask:0xf
	v_add_f32_e32 v1, v1, v10
	s_nop 0
	v_readlane_b32 s1, v1, 63
	s_nop 1
	v_fma_f32 v1, s1, v22, v225
	v_rsq_f32_e32 v10, v1
	s_ashr_i32 s1, s0, 31
	s_lshl_b64 s[0:1], s[0:1], 11
	s_add_u32 s0, s86, s0
	v_pk_mul_f32 v[12:13], v[12:13], v[10:11] op_sel_hi:[1,0]
	v_pk_mul_f32 v[8:9], v[8:9], v[10:11] op_sel_hi:[1,0]
	s_addc_u32 s1, s87, s1
	s_add_i32 s55, s55, s94
	s_cmpk_gt_i32 s55, 0x3ff
	s_waitcnt vmcnt(0)
	v_pk_fma_f32 v[2:3], v[14:15], v[12:13], v[2:3]
	s_nop 0
	v_mul_f32_e32 v1, 0xbfb8aa3b, v2
	v_exp_f32_e32 v1, v1
	v_pk_fma_f32 v[4:5], v[8:9], v[16:17], v[4:5]
	v_add_f32_e32 v1, 1.0, v1
	v_rcp_f32_e32 v12, v1
	v_mul_f32_e32 v1, 0xbfb8aa3b, v3
	v_exp_f32_e32 v1, v1
	s_nop 0
	v_add_f32_e32 v1, 1.0, v1
	v_rcp_f32_e32 v13, v1
	v_mul_f32_e32 v1, 0xbfb8aa3b, v4
	v_exp_f32_e32 v1, v1
	v_pk_mul_f32 v[2:3], v[2:3], v[12:13]
	s_nop 0
	v_cvt_pk_bf16_f32 v2, v2, v3
	v_add_f32_e32 v1, 1.0, v1
	v_rcp_f32_e32 v8, v1
	v_mul_f32_e32 v1, 0xbfb8aa3b, v5
	v_exp_f32_e32 v1, v1
	s_nop 0
	v_add_f32_e32 v1, 1.0, v1
	v_rcp_f32_e32 v9, v1
	s_nop 0
	v_pk_mul_f32 v[4:5], v[4:5], v[8:9]
	s_nop 0
	v_cvt_pk_bf16_f32 v3, v4, v5
	v_lshl_add_u64 v[4:5], s[0:1], 0, v[6:7]
	global_store_dwordx2 v[4:5], v[2:3], off offset:1536
	s_barrier
	s_cbranch_scc0 .LBB0_367
	s_branch .LBB0_412
